# speedup vs baseline: 1.0537x; 1.0044x over previous
_Z9ln_kernelPKfPfS0_S0_:
	s_load_dwordx8 s[4:11], s[0:1], 0x0
	s_mov_b32 s3, 0
	s_lshl_b64 s[2:3], s[2:3], 14
	v_mov_b32_e32 v51, 0
	v_lshlrev_b32_e32 v50, 4, v0
	s_waitcnt lgkmcnt(0)
	s_add_u32 s0, s4, s2
	s_addc_u32 s1, s5, s3
	s_movk_i32 s4, 0x2000
	v_lshl_add_u64 v[2:3], s[0:1], 0, v[50:51]
	v_add_co_u32_e32 v4, vcc, s4, v2
	global_load_dwordx4 v[34:37], v50, s[0:1]
	s_nop 0
	v_addc_co_u32_e32 v5, vcc, 0, v3, vcc
	s_movk_i32 s0, 0x3000
	v_add_co_u32_e32 v2, vcc, s0, v2
	global_load_dwordx4 v[42:45], v[4:5], off offset:-4096
	global_load_dwordx4 v[38:41], v[4:5], off
	v_addc_co_u32_e32 v3, vcc, 0, v3, vcc
	global_load_dwordx4 v[46:49], v[2:3], off
	v_lshl_add_u64 v[2:3], s[8:9], 0, v[50:51]
	v_add_co_u32_e32 v52, vcc, s4, v2
	v_lshl_add_u64 v[4:5], s[10:11], 0, v[50:51]
	s_nop 0
	v_addc_co_u32_e32 v53, vcc, 0, v3, vcc
	v_add_co_u32_e32 v54, vcc, s4, v4
	global_load_dwordx4 v[30:33], v50, s[8:9]
	global_load_dwordx4 v[26:29], v50, s[10:11]
	v_addc_co_u32_e32 v55, vcc, 0, v5, vcc
	v_add_co_u32_e32 v56, vcc, s0, v2
	v_mbcnt_lo_u32_b32 v1, -1, 0
	s_nop 0
	v_addc_co_u32_e32 v57, vcc, 0, v3, vcc
	v_add_co_u32_e32 v58, vcc, s0, v4
	v_mbcnt_hi_u32_b32 v1, -1, v1
	s_nop 0
	v_addc_co_u32_e32 v59, vcc, 0, v5, vcc
	global_load_dwordx4 v[22:25], v[52:53], off offset:-4096
	global_load_dwordx4 v[14:17], v[52:53], off
	global_load_dwordx4 v[18:21], v[54:55], off offset:-4096
	global_load_dwordx4 v[10:13], v[54:55], off
	global_load_dwordx4 v[6:9], v[56:57], off
	global_load_dwordx4 v[2:5], v[58:59], off
	v_and_b32_e32 v52, 64, v1
	v_xor_b32_e32 v53, 32, v1
	v_add_u32_e32 v52, 64, v52
	v_cmp_lt_i32_e32 vcc, v53, v52
	v_xor_b32_e32 v61, 1, v1
	v_and_b32_e32 v50, 63, v0
	v_cndmask_b32_e32 v53, v1, v53, vcc
	v_lshlrev_b32_e32 v55, 2, v53
	v_lshlrev_b32_e32 v54, 2, v0
	s_barrier
	s_waitcnt vmcnt(11)
	v_add_f32_e32 v53, v34, v35
	v_add_f32_e32 v53, v36, v53
	v_add_f32_e32 v53, v37, v53
	v_add_f32_e32 v53, 0, v53
	s_waitcnt vmcnt(10)
	v_add_f32_e32 v56, v42, v43
	s_waitcnt vmcnt(9)
	v_add_f32_e32 v57, v38, v39
	v_add_f32_e32 v56, v44, v56
	v_add_f32_e32 v57, v40, v57
	s_waitcnt vmcnt(8)
	v_add_f32_e32 v58, v46, v47
	v_add_f32_e32 v56, v45, v56
	v_add_f32_e32 v58, v48, v58
	v_add_f32_e32 v57, v41, v57
	v_add_f32_e32 v53, v53, v56
	v_add_f32_e32 v58, v49, v58
	v_add_f32_e32 v53, v53, v57
	v_add_f32_e32 v53, v53, v58
	ds_bpermute_b32 v57, v55, v53
	v_xor_b32_e32 v56, 16, v1
	v_cmp_lt_i32_e32 vcc, v56, v52
	s_waitcnt lgkmcnt(0)
	v_add_f32_e32 v53, v53, v57
	v_cndmask_b32_e32 v56, v1, v56, vcc
	v_lshlrev_b32_e32 v56, 2, v56
	ds_bpermute_b32 v58, v56, v53
	v_xor_b32_e32 v57, 8, v1
	v_cmp_lt_i32_e32 vcc, v57, v52
	s_waitcnt lgkmcnt(0)
	v_add_f32_e32 v53, v53, v58
	v_cndmask_b32_e32 v57, v1, v57, vcc
	v_lshlrev_b32_e32 v57, 2, v57
	ds_bpermute_b32 v59, v57, v53
	v_xor_b32_e32 v58, 4, v1
	v_cmp_lt_i32_e32 vcc, v58, v52
	s_waitcnt lgkmcnt(0)
	v_add_f32_e32 v53, v53, v59
	v_cndmask_b32_e32 v58, v1, v58, vcc
	v_lshlrev_b32_e32 v58, 2, v58
	ds_bpermute_b32 v60, v58, v53
	v_xor_b32_e32 v59, 2, v1
	v_cmp_lt_i32_e32 vcc, v59, v52
	s_waitcnt lgkmcnt(0)
	v_add_f32_e32 v53, v53, v60
	v_cndmask_b32_e32 v59, v1, v59, vcc
	v_lshlrev_b32_e32 v59, 2, v59
	ds_bpermute_b32 v60, v59, v53
	v_cmp_lt_i32_e32 vcc, v61, v52
	s_nop 1
	v_cndmask_b32_e32 v1, v1, v61, vcc
	v_lshlrev_b32_e32 v61, 2, v1
	s_waitcnt lgkmcnt(0)
	v_add_f32_e32 v1, v53, v60
	v_cmp_eq_u32_e32 vcc, 0, v50
	ds_bpermute_b32 v50, v61, v1
	v_lshrrev_b32_e32 v60, 4, v0
	s_and_saveexec_b64 s[0:1], vcc
	s_cbranch_execz .LBB4_2
	s_waitcnt lgkmcnt(0)
	v_add_f32_e32 v0, v1, v50
	ds_write_b32 v60, v0
